# router phase: per-expert slot lists built by wave 0 one row per lane (match masks, popcount, mbcnt rank) instead of 8 lanes walking 64 rows serially; same lists and order
# speedup vs baseline: 1.0150x; 1.0052x over previous
; template <int YMODE, int EXTRA, bool NORM_OUT, bool XN8  , bool XIN_BF = false  , bool XOUT_BF = false  > ...
;     ...
;             if (F.tid < NE) { const int e = F.tid; int c = 0;
;                 for (int r = 0; r < 64; ++r) c += (routei[r * 4] == e) + (routei[r * 4 + 1] == e);
;                 int base = (int)__hip_atomic_fetch_add(cntw + e, (unsigned)c, __ATOMIC_RELAXED, __HIP_MEMORY_SCOPE_AGENT);
;                 float* rms = rowmax + (WS_RMSLOT - WS_ROWMAX) / 4;
;                 for (int r = 0; r < 64; ++r) { if (routei[r * 4] == e) { idx_out[e * ECAP + base] = blk * 64 + r; rms[e * ECAP + base] = route[384 + r]; routei[256 + r * 2] = base; ++base; }
;                                                if (routei[r * 4 + 1] == e) { idx_out[e * ECAP + base] = blk * 64 + r; rms[e * ECAP + base] = route[384 + r]; routei[256 + r * 2 + 1] = base; ++base; } } }
.LBB0_2183:
	s_waitcnt lgkmcnt(0)
	s_barrier
	s_and_saveexec_b64 s[0:1], s[10:11]
	s_cbranch_execz .LBB0_2194
	v_lshlrev_b32_e32 v24, 4, v0
	v_add_u32_e32 v24, 0x16000, v24
	ds_read_b64 v[26:27], v24
	v_lshlrev_b32_e32 v25, 2, v0
	v_add_u32_e32 v25, 0x16600, v25
	ds_read_b32 v28, v25
	v_mov_b32_e32 v29, 0
	v_lshlrev_b32_e32 v25, 3, v0
	v_add_u32_e32 v25, 0x16400, v25
	v_mov_b32_e32 v185, 0
	v_add_u32_e32 v2, s33, v0
	s_waitcnt lgkmcnt(0)
	v_cmp_eq_u32_e64 s[12:13], v26, 0
	v_cmp_eq_u32_e64 s[14:15], v27, 0
	s_or_b64 s[12:13], s[12:13], s[14:15]
	s_bcnt1_i32_b64 s16, s[12:13]
	v_writelane_b32 v29, s16, 0
	v_cmp_eq_u32_e64 s[12:13], v26, 1
	v_cmp_eq_u32_e64 s[14:15], v27, 1
	s_or_b64 s[12:13], s[12:13], s[14:15]
	s_bcnt1_i32_b64 s16, s[12:13]
	v_writelane_b32 v29, s16, 1
	v_cmp_eq_u32_e64 s[12:13], v26, 2
	v_cmp_eq_u32_e64 s[14:15], v27, 2
	s_or_b64 s[12:13], s[12:13], s[14:15]
	s_bcnt1_i32_b64 s16, s[12:13]
	v_writelane_b32 v29, s16, 2
	v_cmp_eq_u32_e64 s[12:13], v26, 3
	v_cmp_eq_u32_e64 s[14:15], v27, 3
	s_or_b64 s[12:13], s[12:13], s[14:15]
	s_bcnt1_i32_b64 s16, s[12:13]
	v_writelane_b32 v29, s16, 3
	v_cmp_eq_u32_e64 s[12:13], v26, 4
	v_cmp_eq_u32_e64 s[14:15], v27, 4
	s_or_b64 s[12:13], s[12:13], s[14:15]
	s_bcnt1_i32_b64 s16, s[12:13]
	v_writelane_b32 v29, s16, 4
	v_cmp_eq_u32_e64 s[12:13], v26, 5
	v_cmp_eq_u32_e64 s[14:15], v27, 5
	s_or_b64 s[12:13], s[12:13], s[14:15]
	s_bcnt1_i32_b64 s16, s[12:13]
	v_writelane_b32 v29, s16, 5
	v_cmp_eq_u32_e64 s[12:13], v26, 6
	v_cmp_eq_u32_e64 s[14:15], v27, 6
	s_or_b64 s[12:13], s[12:13], s[14:15]
	s_bcnt1_i32_b64 s16, s[12:13]
	v_writelane_b32 v29, s16, 6
	v_cmp_eq_u32_e64 s[12:13], v26, 7
	v_cmp_eq_u32_e64 s[14:15], v27, 7
	s_or_b64 s[12:13], s[12:13], s[14:15]
	s_bcnt1_i32_b64 s16, s[12:13]
	v_writelane_b32 v29, s16, 7
	s_and_b64 exec, exec, s[8:9]
	global_atomic_add v30, v[18:19], v29, off offset:256 sc0
	s_mov_b64 exec, s[10:11]
	s_waitcnt vmcnt(0)
	v_cmp_eq_u32_e64 s[12:13], v26, 0
	v_cmp_eq_u32_e64 s[14:15], v27, 0
	v_readlane_b32 s18, v30, 0
	s_or_b64 s[16:17], s[12:13], s[14:15]
	v_mbcnt_lo_u32_b32 v31, s16, 0
	v_mbcnt_hi_u32_b32 v31, s17, v31
	v_cndmask_b32_e64 v24, 0, 4, s[14:15]
	v_add_u32_e32 v31, s18, v31
	v_add_u32_e32 v24, v25, v24
	s_and_b64 exec, exec, s[16:17]
	v_mov_b32_e32 v184, v31
	v_lshlrev_b32_e32 v184, 2, v184
	v_lshl_add_u64 v[186:187], s[30:31], 0, v[184:185]
	v_lshl_add_u64 v[188:189], s[36:37], 0, v[184:185]
	global_store_dword v[186:187], v2, off
	global_store_dword v[188:189], v28, off
	ds_write_b32 v24, v31
	s_mov_b64 exec, s[10:11]
	v_cmp_eq_u32_e64 s[12:13], v26, 1
	v_cmp_eq_u32_e64 s[14:15], v27, 1
	v_readlane_b32 s18, v30, 1
	s_or_b64 s[16:17], s[12:13], s[14:15]
	v_mbcnt_lo_u32_b32 v31, s16, 0
	v_mbcnt_hi_u32_b32 v31, s17, v31
	v_cndmask_b32_e64 v24, 0, 4, s[14:15]
	v_add_u32_e32 v31, s18, v31
	v_add_u32_e32 v24, v25, v24
	s_and_b64 exec, exec, s[16:17]
	v_add_u32_e32 v184, 0x4000, v31
	v_lshlrev_b32_e32 v184, 2, v184
	v_lshl_add_u64 v[186:187], s[30:31], 0, v[184:185]
	v_lshl_add_u64 v[188:189], s[36:37], 0, v[184:185]
	global_store_dword v[186:187], v2, off
	global_store_dword v[188:189], v28, off
	ds_write_b32 v24, v31
	s_mov_b64 exec, s[10:11]
	v_cmp_eq_u32_e64 s[12:13], v26, 2
	v_cmp_eq_u32_e64 s[14:15], v27, 2
	v_readlane_b32 s18, v30, 2
	s_or_b64 s[16:17], s[12:13], s[14:15]
	v_mbcnt_lo_u32_b32 v31, s16, 0
	v_mbcnt_hi_u32_b32 v31, s17, v31
	v_cndmask_b32_e64 v24, 0, 4, s[14:15]
	v_add_u32_e32 v31, s18, v31
	v_add_u32_e32 v24, v25, v24
	s_and_b64 exec, exec, s[16:17]
	v_add_u32_e32 v184, 0x8000, v31
	v_lshlrev_b32_e32 v184, 2, v184
	v_lshl_add_u64 v[186:187], s[30:31], 0, v[184:185]
	v_lshl_add_u64 v[188:189], s[36:37], 0, v[184:185]
	global_store_dword v[186:187], v2, off
	global_store_dword v[188:189], v28, off
	ds_write_b32 v24, v31
	s_mov_b64 exec, s[10:11]
	v_cmp_eq_u32_e64 s[12:13], v26, 3
	v_cmp_eq_u32_e64 s[14:15], v27, 3
	v_readlane_b32 s18, v30, 3
	s_or_b64 s[16:17], s[12:13], s[14:15]
	v_mbcnt_lo_u32_b32 v31, s16, 0
	v_mbcnt_hi_u32_b32 v31, s17, v31
	v_cndmask_b32_e64 v24, 0, 4, s[14:15]
	v_add_u32_e32 v31, s18, v31
	v_add_u32_e32 v24, v25, v24
	s_and_b64 exec, exec, s[16:17]
	v_add_u32_e32 v184, 0xc000, v31
	v_lshlrev_b32_e32 v184, 2, v184
	v_lshl_add_u64 v[186:187], s[30:31], 0, v[184:185]
	v_lshl_add_u64 v[188:189], s[36:37], 0, v[184:185]
	global_store_dword v[186:187], v2, off
	global_store_dword v[188:189], v28, off
	ds_write_b32 v24, v31
	s_mov_b64 exec, s[10:11]
	v_cmp_eq_u32_e64 s[12:13], v26, 4
	v_cmp_eq_u32_e64 s[14:15], v27, 4
	v_readlane_b32 s18, v30, 4
	s_or_b64 s[16:17], s[12:13], s[14:15]
	v_mbcnt_lo_u32_b32 v31, s16, 0
	v_mbcnt_hi_u32_b32 v31, s17, v31
	v_cndmask_b32_e64 v24, 0, 4, s[14:15]
	v_add_u32_e32 v31, s18, v31
	v_add_u32_e32 v24, v25, v24
	s_and_b64 exec, exec, s[16:17]
	v_add_u32_e32 v184, 0x10000, v31
	v_lshlrev_b32_e32 v184, 2, v184
	v_lshl_add_u64 v[186:187], s[30:31], 0, v[184:185]
	v_lshl_add_u64 v[188:189], s[36:37], 0, v[184:185]
	global_store_dword v[186:187], v2, off
	global_store_dword v[188:189], v28, off
	ds_write_b32 v24, v31
	s_mov_b64 exec, s[10:11]
	v_cmp_eq_u32_e64 s[12:13], v26, 5
	v_cmp_eq_u32_e64 s[14:15], v27, 5
	v_readlane_b32 s18, v30, 5
	s_or_b64 s[16:17], s[12:13], s[14:15]
	v_mbcnt_lo_u32_b32 v31, s16, 0
	v_mbcnt_hi_u32_b32 v31, s17, v31
	v_cndmask_b32_e64 v24, 0, 4, s[14:15]
	v_add_u32_e32 v31, s18, v31
	v_add_u32_e32 v24, v25, v24
	s_and_b64 exec, exec, s[16:17]
	v_add_u32_e32 v184, 0x14000, v31
	v_lshlrev_b32_e32 v184, 2, v184
	v_lshl_add_u64 v[186:187], s[30:31], 0, v[184:185]
	v_lshl_add_u64 v[188:189], s[36:37], 0, v[184:185]
	global_store_dword v[186:187], v2, off
	global_store_dword v[188:189], v28, off
	ds_write_b32 v24, v31
	s_mov_b64 exec, s[10:11]
	v_cmp_eq_u32_e64 s[12:13], v26, 6
	v_cmp_eq_u32_e64 s[14:15], v27, 6
	v_readlane_b32 s18, v30, 6
	s_or_b64 s[16:17], s[12:13], s[14:15]
	v_mbcnt_lo_u32_b32 v31, s16, 0
	v_mbcnt_hi_u32_b32 v31, s17, v31
	v_cndmask_b32_e64 v24, 0, 4, s[14:15]
	v_add_u32_e32 v31, s18, v31
	v_add_u32_e32 v24, v25, v24
	s_and_b64 exec, exec, s[16:17]
	v_add_u32_e32 v184, 0x18000, v31
	v_lshlrev_b32_e32 v184, 2, v184
	v_lshl_add_u64 v[186:187], s[30:31], 0, v[184:185]
	v_lshl_add_u64 v[188:189], s[36:37], 0, v[184:185]
	global_store_dword v[186:187], v2, off
	global_store_dword v[188:189], v28, off
	ds_write_b32 v24, v31
	s_mov_b64 exec, s[10:11]
	v_cmp_eq_u32_e64 s[12:13], v26, 7
	v_cmp_eq_u32_e64 s[14:15], v27, 7
	v_readlane_b32 s18, v30, 7
	s_or_b64 s[16:17], s[12:13], s[14:15]
	v_mbcnt_lo_u32_b32 v31, s16, 0
	v_mbcnt_hi_u32_b32 v31, s17, v31
	v_cndmask_b32_e64 v24, 0, 4, s[14:15]
	v_add_u32_e32 v31, s18, v31
	v_add_u32_e32 v24, v25, v24
	s_and_b64 exec, exec, s[16:17]
	v_add_u32_e32 v184, 0x1c000, v31
	v_lshlrev_b32_e32 v184, 2, v184
	v_lshl_add_u64 v[186:187], s[30:31], 0, v[184:185]
	v_lshl_add_u64 v[188:189], s[36:37], 0, v[184:185]
	global_store_dword v[186:187], v2, off
	global_store_dword v[188:189], v28, off
	ds_write_b32 v24, v31
	s_mov_b64 exec, s[10:11]
